# main-loop entry labels of the four GEMM kernels pinned to 64-byte boundaries (code placement)
# baseline (speedup 1.0000x reference)
.LBB2_32:
	s_xor_b64 s[30:31], s[4:5], -1
	s_lshl_b32 s4, s63, 8
	s_ashr_i32 s5, s4, 31
	s_lshl_b64 s[4:5], s[4:5], 11
	s_add_u32 s4, s14, s4
	s_addc_u32 s5, s15, s5
	s_add_u32 s24, s4, 0x400000
	s_addc_u32 s25, s5, 0
	s_and_b64 s[4:5], s[28:29], exec
	s_cselect_b32 s66, s25, s19
	s_cselect_b32 s67, s24, s18
	s_lshl_b32 s4, s62, 8
	s_ashr_i32 s5, s4, 31
	s_lshl_b64 s[4:5], s[4:5], 11
	s_add_u32 s26, s12, s4
	s_addc_u32 s27, s13, s5
	s_and_b64 s[4:5], s[28:29], exec
	s_cselect_b32 s68, s27, s1
	s_cselect_b32 s69, s26, s0
	s_add_u32 s70, s18, 0x40080
	s_addc_u32 s71, s19, 0
	s_add_u32 s72, s0, 0x100
	v_mov_b64_e32 v[0:1], 0
	s_addc_u32 s73, s1, 0
	s_mov_b32 s74, -2
	v_mov_b64_e32 v[2:3], 0
	v_mov_b64_e32 v[4:5], 0
	v_mov_b64_e32 v[6:7], 0
	v_mov_b64_e32 v[8:9], 0
	v_mov_b64_e32 v[10:11], 0
	v_mov_b64_e32 v[12:13], 0
	v_mov_b64_e32 v[14:15], 0
	v_mov_b64_e32 v[16:17], 0
	v_mov_b64_e32 v[18:19], 0
	v_mov_b64_e32 v[20:21], 0
	v_mov_b64_e32 v[22:23], 0
	v_mov_b64_e32 v[24:25], 0
	v_mov_b64_e32 v[26:27], 0
	v_mov_b64_e32 v[28:29], 0
	v_mov_b64_e32 v[30:31], 0
	v_mov_b64_e32 v[32:33], 0
	v_mov_b64_e32 v[34:35], 0
	v_mov_b64_e32 v[36:37], 0
	v_mov_b64_e32 v[38:39], 0
	v_mov_b64_e32 v[40:41], 0
	v_mov_b64_e32 v[42:43], 0
	v_mov_b64_e32 v[44:45], 0
	v_mov_b64_e32 v[46:47], 0
	v_mov_b64_e32 v[48:49], 0
	v_mov_b64_e32 v[50:51], 0
	v_mov_b64_e32 v[52:53], 0
	v_mov_b64_e32 v[54:55], 0
	v_mov_b64_e32 v[56:57], 0
	v_mov_b64_e32 v[58:59], 0
	v_mov_b64_e32 v[60:61], 0
	v_mov_b64_e32 v[62:63], 0
	v_mov_b64_e32 v[64:65], 0
	v_mov_b64_e32 v[66:67], 0
	v_mov_b64_e32 v[68:69], 0
	v_mov_b64_e32 v[70:71], 0
	v_mov_b64_e32 v[72:73], 0
	v_mov_b64_e32 v[74:75], 0
	v_mov_b64_e32 v[76:77], 0
	v_mov_b64_e32 v[78:79], 0
	v_mov_b64_e32 v[80:81], 0
	v_mov_b64_e32 v[82:83], 0
	v_mov_b64_e32 v[84:85], 0
	v_mov_b64_e32 v[86:87], 0
	v_mov_b64_e32 v[88:89], 0
	v_mov_b64_e32 v[90:91], 0
	v_mov_b64_e32 v[92:93], 0
	v_mov_b64_e32 v[94:95], 0
	v_mov_b64_e32 v[96:97], 0
	v_mov_b64_e32 v[98:99], 0
	v_mov_b64_e32 v[100:101], 0
	v_mov_b64_e32 v[102:103], 0
	v_mov_b64_e32 v[104:105], 0
	v_mov_b64_e32 v[106:107], 0
	v_mov_b64_e32 v[108:109], 0
	v_mov_b64_e32 v[110:111], 0
	v_mov_b64_e32 v[112:113], 0
	v_mov_b64_e32 v[114:115], 0
	v_mov_b64_e32 v[116:117], 0
	v_mov_b64_e32 v[118:119], 0
	v_mov_b64_e32 v[120:121], 0
	v_mov_b64_e32 v[122:123], 0
	v_mov_b64_e32 v[124:125], 0
	v_mov_b64_e32 v[126:127], 0
	s_waitcnt lgkmcnt(0)
	v_add_u32_e32 v212, 0x1c000, v199
	v_add_u32_e32 v213, 0x1c000, v200
	s_branch .LBB2_34
	.p2align	6

.Lp2_sum_skip:
	s_barrier
	buffer_load_dwordx4 v194, s[12:15], 0 offen lds
	s_mov_b32 m0, s41
	v_lshrrev_b32_e32 v2, 4, v0
	buffer_load_dwordx4 v196, s[12:15], 0 offen lds
	s_add_u32 s12, s16, 0x80
	s_addc_u32 s0, s9, 0
	s_add_i32 s42, s31, 0x8000
	s_and_b32 s13, s0, 0xffff
	s_mov_b32 m0, s42
	s_add_i32 s43, s31, 0xa000
	buffer_load_dwordx4 v1, s[12:15], 0 offen lds
	s_mov_b32 m0, s43
	v_and_b32_e32 v197, 15, v0
	buffer_load_dwordx4 v195, s[12:15], 0 offen lds
	s_add_u32 s12, s8, 0x10080
	s_addc_u32 s0, s25, 0
	s_add_i32 s44, s31, 0x1c000
	s_and_b32 s13, s0, 0xffff
	s_mov_b32 m0, s44
	s_add_i32 s45, s31, 0x1e000
	buffer_load_dwordx4 v194, s[12:15], 0 offen lds
	s_mov_b32 m0, s45
	s_and_b32 s0, s2, 1
	buffer_load_dwordx4 v196, s[12:15], 0 offen lds
	s_lshl_b32 s0, s0, 23
	s_lshl_b32 s1, s26, 21
	v_bfe_u32 v3, v0, 1, 3
	s_or_b32 s0, s0, s1
	v_bitop3_b32 v2, v2, v3, 3 bitop3:0x6c
	v_lshlrev_b32_e32 v3, 7, v197
	s_add_i32 s46, s31, 0xc000
	s_add_i32 s47, s31, 0xe000
	s_or_b32 s0, s27, s0
	v_lshlrev_b32_e32 v2, 4, v2
	v_lshl_or_b32 v4, s28, 13, v3
	v_lshl_or_b32 v3, s39, 12, v3
	s_waitcnt vmcnt(6)
	s_add_u32 s48, s20, s0
	v_or_b32_e32 v5, v4, v2
	v_bitop3_b32 v4, v4, 64, v2 bitop3:0x36
	v_or_b32_e32 v198, v3, v2
	v_bitop3_b32 v199, v3, 64, v2 bitop3:0x36
	s_addc_u32 s49, s21, 0
	v_mov_b32_e32 v66, 0
	s_add_i32 s0, 0, 0x10000
	s_add_i32 s1, 0, 0x14000
	s_mov_b32 s50, -2
	s_mov_b64 s[10:11], 0
	v_add_u32_e32 v200, 0, v5
	v_add_u32_e32 v201, 0, v4
	v_mov_b32_e32 v67, v66
	v_mov_b32_e32 v68, v66
	v_mov_b32_e32 v69, v66
	v_mov_b32_e32 v70, v66
	v_mov_b32_e32 v71, v66
	v_mov_b32_e32 v72, v66
	v_mov_b32_e32 v73, v66
	v_mov_b32_e32 v82, v66
	v_mov_b32_e32 v83, v66
	v_mov_b32_e32 v84, v66
	v_mov_b32_e32 v85, v66
	v_mov_b32_e32 v86, v66
	v_mov_b32_e32 v87, v66
	v_mov_b32_e32 v88, v66
	v_mov_b32_e32 v89, v66
	v_mov_b32_e32 v98, v66
	v_mov_b32_e32 v99, v66
	v_mov_b32_e32 v100, v66
	v_mov_b32_e32 v101, v66
	v_mov_b32_e32 v102, v66
	v_mov_b32_e32 v103, v66
	v_mov_b32_e32 v104, v66
	v_mov_b32_e32 v105, v66
	v_mov_b32_e32 v114, v66
	v_mov_b32_e32 v115, v66
	v_mov_b32_e32 v116, v66
	v_mov_b32_e32 v117, v66
	v_mov_b32_e32 v118, v66
	v_mov_b32_e32 v119, v66
	v_mov_b32_e32 v120, v66
	v_mov_b32_e32 v121, v66
	v_mov_b32_e32 v74, v66
	v_mov_b32_e32 v75, v66
	v_mov_b32_e32 v76, v66
	v_mov_b32_e32 v77, v66
	v_mov_b32_e32 v78, v66
	v_mov_b32_e32 v79, v66
	v_mov_b32_e32 v80, v66
	v_mov_b32_e32 v81, v66
	v_mov_b32_e32 v90, v66
	v_mov_b32_e32 v91, v66
	v_mov_b32_e32 v92, v66
	v_mov_b32_e32 v93, v66
	v_mov_b32_e32 v94, v66
	v_mov_b32_e32 v95, v66
	v_mov_b32_e32 v96, v66
	v_mov_b32_e32 v97, v66
	v_mov_b32_e32 v106, v66
	v_mov_b32_e32 v107, v66
	v_mov_b32_e32 v108, v66
	v_mov_b32_e32 v109, v66
	v_mov_b32_e32 v110, v66
	v_mov_b32_e32 v111, v66
	v_mov_b32_e32 v112, v66
	v_mov_b32_e32 v113, v66
	v_mov_b32_e32 v122, v66
	v_mov_b32_e32 v123, v66
	v_mov_b32_e32 v124, v66
	v_mov_b32_e32 v125, v66
	v_mov_b32_e32 v126, v66
	v_mov_b32_e32 v127, v66
	v_mov_b32_e32 v128, v66
	v_mov_b32_e32 v129, v66
	v_mov_b32_e32 v130, v66
	v_mov_b32_e32 v131, v66
	v_mov_b32_e32 v132, v66
	v_mov_b32_e32 v133, v66
	v_mov_b32_e32 v134, v66
	v_mov_b32_e32 v135, v66
	v_mov_b32_e32 v136, v66
	v_mov_b32_e32 v137, v66
	v_mov_b32_e32 v146, v66
	v_mov_b32_e32 v147, v66
	v_mov_b32_e32 v148, v66
	v_mov_b32_e32 v149, v66
	v_mov_b32_e32 v150, v66
	v_mov_b32_e32 v151, v66
	v_mov_b32_e32 v152, v66
	v_mov_b32_e32 v153, v66
	v_mov_b32_e32 v162, v66
	v_mov_b32_e32 v163, v66
	v_mov_b32_e32 v164, v66
	v_mov_b32_e32 v165, v66
	v_mov_b32_e32 v166, v66
	v_mov_b32_e32 v167, v66
	v_mov_b32_e32 v168, v66
	v_mov_b32_e32 v169, v66
	v_mov_b32_e32 v178, v66
	v_mov_b32_e32 v179, v66
	v_mov_b32_e32 v180, v66
	v_mov_b32_e32 v181, v66
	v_mov_b32_e32 v182, v66
	v_mov_b32_e32 v183, v66
	v_mov_b32_e32 v184, v66
	v_mov_b32_e32 v185, v66
	v_mov_b32_e32 v138, v66
	v_mov_b32_e32 v139, v66
	v_mov_b32_e32 v140, v66
	v_mov_b32_e32 v141, v66
	v_mov_b32_e32 v142, v66
	v_mov_b32_e32 v143, v66
	v_mov_b32_e32 v144, v66
	v_mov_b32_e32 v145, v66
	v_mov_b32_e32 v154, v66
	v_mov_b32_e32 v155, v66
	v_mov_b32_e32 v156, v66
	v_mov_b32_e32 v157, v66
	v_mov_b32_e32 v158, v66
	v_mov_b32_e32 v159, v66
	v_mov_b32_e32 v160, v66
	v_mov_b32_e32 v161, v66
	v_mov_b32_e32 v170, v66
	v_mov_b32_e32 v171, v66
	v_mov_b32_e32 v172, v66
	v_mov_b32_e32 v173, v66
	v_mov_b32_e32 v174, v66
	v_mov_b32_e32 v175, v66
	v_mov_b32_e32 v176, v66
	v_mov_b32_e32 v177, v66
	v_mov_b32_e32 v186, v66
	v_mov_b32_e32 v187, v66
	v_mov_b32_e32 v188, v66
	v_mov_b32_e32 v189, v66
	v_mov_b32_e32 v190, v66
	v_mov_b32_e32 v191, v66
	v_mov_b32_e32 v192, v66
	v_mov_b32_e32 v193, v66
	v_bfe_u32 v202, v0, 4, 2
	v_add_u32_e32 v203, s0, v198
	v_add_u32_e32 v204, s0, v199
	v_add_u32_e32 v205, s1, v198
	v_add_u32_e32 v206, s1, v199
	s_barrier
	s_cmpk_eq_i32 s10, 0x700
	s_cselect_b64 s[18:19], -1, 0
	s_cmpk_lg_i32 s10, 0x700
	s_cselect_b64 s[26:27], -1, 0
	s_add_u32 s54, s48, s10
	s_addc_u32 s55, s49, s11
	s_add_u32 s51, s8, s10
	s_addc_u32 s52, s25, s11
	s_add_u32 s20, s51, 0x100
	s_addc_u32 s53, s52, 0
	s_add_u32 s12, s54, 0x100080
	s_addc_u32 s0, s55, 0
	s_and_b32 s13, s0, 0xffff
	v_add_u32_e32 v210, 0x1c000, v198
	v_add_u32_e32 v211, 0x1c000, v199
	s_branch .LBB3_4
	.p2align	6

.LBB4_12:
	s_and_b32 s33, s0, 3
	s_add_u32 s12, s8, 0x80
	s_addc_u32 s0, s3, 0
	s_add_i32 s36, s7, 0x18000
	s_and_b32 s13, s0, 0xffff
	s_mov_b32 m0, s36
	s_add_i32 s37, s7, 0x1a000
	s_waitcnt vmcnt(4)
	s_barrier
	buffer_load_dwordx4 v193, s[12:15], 0 offen lds
	s_mov_b32 m0, s37
	v_lshrrev_b32_e32 v1, 4, v0
	buffer_load_dwordx4 v195, s[12:15], 0 offen lds
	s_add_u32 s12, s16, 0x80
	s_addc_u32 s0, s9, 0
	s_add_i32 s38, s7, 0x8000
	s_and_b32 s13, s0, 0xffff
	s_mov_b32 m0, s38
	s_add_i32 s39, s7, 0xa000
	buffer_load_dwordx4 v192, s[12:15], 0 offen lds
	s_mov_b32 m0, s39
	v_and_b32_e32 v196, 15, v0
	buffer_load_dwordx4 v194, s[12:15], 0 offen lds
	s_add_u32 s12, s8, 0x4080
	s_addc_u32 s0, s3, 0
	s_add_i32 s40, s7, 0x1c000
	s_and_b32 s13, s0, 0xffff
	s_mov_b32 m0, s40
	s_add_i32 s41, s7, 0x1e000
	buffer_load_dwordx4 v193, s[12:15], 0 offen lds
	s_mov_b32 m0, s41
	v_bfe_u32 v197, v0, 4, 2
	buffer_load_dwordx4 v195, s[12:15], 0 offen lds
	v_bfe_u32 v0, v0, 1, 3
	v_bitop3_b32 v0, v1, v0, 3 bitop3:0x6c
	v_lshlrev_b32_e32 v1, 7, v196
	v_lshlrev_b32_e32 v0, 4, v0
	v_lshl_or_b32 v2, s27, 13, v1
	v_lshl_or_b32 v1, s33, 12, v1
	s_waitcnt vmcnt(6)
	v_or_b32_e32 v3, v2, v0
	v_or_b32_e32 v198, v1, v0
	v_bitop3_b32 v2, v2, 64, v0 bitop3:0x36
	v_bitop3_b32 v199, v1, 64, v0 bitop3:0x36
	v_mov_b32_e32 v64, 0
	s_add_i32 s0, 0, 0x10000
	s_add_i32 s1, 0, 0x14000
	s_add_i32 s42, s7, 0xc000
	s_add_i32 s43, s7, 0xe000
	s_mov_b32 s44, -2
	s_mov_b64 s[10:11], 0
	v_add_u32_e32 v200, 0, v3
	v_add_u32_e32 v201, 0, v2
	s_add_i32 s45, 0, 0x18000
	v_mov_b32_e32 v65, v64
	v_mov_b32_e32 v66, v64
	v_mov_b32_e32 v67, v64
	v_mov_b32_e32 v68, v64
	v_mov_b32_e32 v69, v64
	v_mov_b32_e32 v70, v64
	v_mov_b32_e32 v71, v64
	v_mov_b32_e32 v80, v64
	v_mov_b32_e32 v81, v64
	v_mov_b32_e32 v82, v64
	v_mov_b32_e32 v83, v64
	v_mov_b32_e32 v84, v64
	v_mov_b32_e32 v85, v64
	v_mov_b32_e32 v86, v64
	v_mov_b32_e32 v87, v64
	v_mov_b32_e32 v96, v64
	v_mov_b32_e32 v97, v64
	v_mov_b32_e32 v98, v64
	v_mov_b32_e32 v99, v64
	v_mov_b32_e32 v100, v64
	v_mov_b32_e32 v101, v64
	v_mov_b32_e32 v102, v64
	v_mov_b32_e32 v103, v64
	v_mov_b32_e32 v112, v64
	v_mov_b32_e32 v113, v64
	v_mov_b32_e32 v114, v64
	v_mov_b32_e32 v115, v64
	v_mov_b32_e32 v116, v64
	v_mov_b32_e32 v117, v64
	v_mov_b32_e32 v118, v64
	v_mov_b32_e32 v119, v64
	v_mov_b32_e32 v72, v64
	v_mov_b32_e32 v73, v64
	v_mov_b32_e32 v74, v64
	v_mov_b32_e32 v75, v64
	v_mov_b32_e32 v76, v64
	v_mov_b32_e32 v77, v64
	v_mov_b32_e32 v78, v64
	v_mov_b32_e32 v79, v64
	v_mov_b32_e32 v88, v64
	v_mov_b32_e32 v89, v64
	v_mov_b32_e32 v90, v64
	v_mov_b32_e32 v91, v64
	v_mov_b32_e32 v92, v64
	v_mov_b32_e32 v93, v64
	v_mov_b32_e32 v94, v64
	v_mov_b32_e32 v95, v64
	v_mov_b32_e32 v104, v64
	v_mov_b32_e32 v105, v64
	v_mov_b32_e32 v106, v64
	v_mov_b32_e32 v107, v64
	v_mov_b32_e32 v108, v64
	v_mov_b32_e32 v109, v64
	v_mov_b32_e32 v110, v64
	v_mov_b32_e32 v111, v64
	v_mov_b32_e32 v120, v64
	v_mov_b32_e32 v121, v64
	v_mov_b32_e32 v122, v64
	v_mov_b32_e32 v123, v64
	v_mov_b32_e32 v124, v64
	v_mov_b32_e32 v125, v64
	v_mov_b32_e32 v126, v64
	v_mov_b32_e32 v127, v64
	v_mov_b32_e32 v128, v64
	v_mov_b32_e32 v129, v64
	v_mov_b32_e32 v130, v64
	v_mov_b32_e32 v131, v64
	v_mov_b32_e32 v132, v64
	v_mov_b32_e32 v133, v64
	v_mov_b32_e32 v134, v64
	v_mov_b32_e32 v135, v64
	v_mov_b32_e32 v144, v64
	v_mov_b32_e32 v145, v64
	v_mov_b32_e32 v146, v64
	v_mov_b32_e32 v147, v64
	v_mov_b32_e32 v148, v64
	v_mov_b32_e32 v149, v64
	v_mov_b32_e32 v150, v64
	v_mov_b32_e32 v151, v64
	v_mov_b32_e32 v160, v64
	v_mov_b32_e32 v161, v64
	v_mov_b32_e32 v162, v64
	v_mov_b32_e32 v163, v64
	v_mov_b32_e32 v164, v64
	v_mov_b32_e32 v165, v64
	v_mov_b32_e32 v166, v64
	v_mov_b32_e32 v167, v64
	v_mov_b32_e32 v176, v64
	v_mov_b32_e32 v177, v64
	v_mov_b32_e32 v178, v64
	v_mov_b32_e32 v179, v64
	v_mov_b32_e32 v180, v64
	v_mov_b32_e32 v181, v64
	v_mov_b32_e32 v182, v64
	v_mov_b32_e32 v183, v64
	v_mov_b32_e32 v136, v64
	v_mov_b32_e32 v137, v64
	v_mov_b32_e32 v138, v64
	v_mov_b32_e32 v139, v64
	v_mov_b32_e32 v140, v64
	v_mov_b32_e32 v141, v64
	v_mov_b32_e32 v142, v64
	v_mov_b32_e32 v143, v64
	v_mov_b32_e32 v152, v64
	v_mov_b32_e32 v153, v64
	v_mov_b32_e32 v154, v64
	v_mov_b32_e32 v155, v64
	v_mov_b32_e32 v156, v64
	v_mov_b32_e32 v157, v64
	v_mov_b32_e32 v158, v64
	v_mov_b32_e32 v159, v64
	v_mov_b32_e32 v168, v64
	v_mov_b32_e32 v169, v64
	v_mov_b32_e32 v170, v64
	v_mov_b32_e32 v171, v64
	v_mov_b32_e32 v172, v64
	v_mov_b32_e32 v173, v64
	v_mov_b32_e32 v174, v64
	v_mov_b32_e32 v175, v64
	v_mov_b32_e32 v184, v64
	v_mov_b32_e32 v185, v64
	v_mov_b32_e32 v186, v64
	v_mov_b32_e32 v187, v64
	v_mov_b32_e32 v188, v64
	v_mov_b32_e32 v189, v64
	v_mov_b32_e32 v190, v64
	v_mov_b32_e32 v191, v64
	v_add_u32_e32 v202, s0, v198
	v_add_u32_e32 v203, s0, v199
	v_add_u32_e32 v204, s1, v198
	v_add_u32_e32 v205, s1, v199
	s_barrier
	s_cmpk_eq_i32 s10, 0x700
	s_cselect_b64 s[18:19], -1, 0
	s_cmpk_lg_i32 s10, 0x700
	s_cselect_b64 s[24:25], -1, 0
	s_add_u32 s49, s16, s10
	s_addc_u32 s50, s9, s11
	s_add_u32 s46, s8, s10
	s_addc_u32 s47, s3, s11
	s_add_u32 s20, s46, 0x100
	s_addc_u32 s48, s47, 0
	s_add_u32 s12, s49, 0x40080
	s_addc_u32 s0, s50, 0
	s_and_b32 s13, s0, 0xffff
	v_add_u32_e32 v207, 0x1c000, v198
	v_add_u32_e32 v208, 0x1c000, v199
	s_branch .LBB4_14
	.p2align	6

.LBB5_16:
	s_and_b32 s35, s20, 3
	s_add_u32 s8, s12, 0x80
	s_load_dword s2, s[0:1], 0x48
	s_addc_u32 s0, s7, 0
	s_add_i32 s37, s25, 0x18000
	s_and_b32 s9, s0, 0xffff
	s_mov_b32 m0, s37
	s_add_i32 s38, s25, 0x1a000
	s_waitcnt vmcnt(4)
	s_barrier
	buffer_load_dwordx4 v192, s[8:11], 0 offen lds
	s_mov_b32 m0, s38
	v_lshrrev_b32_e32 v1, 4, v0
	buffer_load_dwordx4 v193, s[8:11], 0 offen lds
	s_add_u32 s8, s16, 0x80
	s_addc_u32 s0, s13, 0
	s_add_i32 s39, s25, 0x8000
	s_and_b32 s9, s0, 0xffff
	s_mov_b32 m0, s39
	s_add_i32 s40, s25, 0xa000
	buffer_load_dwordx4 v192, s[8:11], 0 offen lds
	s_mov_b32 m0, s40
	v_and_b32_e32 v194, 15, v0
	buffer_load_dwordx4 v193, s[8:11], 0 offen lds
	s_add_u32 s8, s12, 0x40080
	s_addc_u32 s0, s7, 0
	s_add_i32 s41, s25, 0x1c000
	s_and_b32 s9, s0, 0xffff
	s_mov_b32 m0, s41
	s_add_i32 s42, s25, 0x1e000
	buffer_load_dwordx4 v192, s[8:11], 0 offen lds
	s_mov_b32 m0, s42
	v_bfe_u32 v195, v0, 4, 2
	buffer_load_dwordx4 v193, s[8:11], 0 offen lds
	v_bfe_u32 v0, v0, 1, 3
	v_bitop3_b32 v0, v1, v0, 3 bitop3:0x6c
	v_lshlrev_b32_e32 v1, 7, v194
	v_lshlrev_b32_e32 v0, 4, v0
	v_lshl_or_b32 v2, s3, 13, v1
	v_lshl_or_b32 v1, s35, 12, v1
	s_waitcnt vmcnt(6)
	v_or_b32_e32 v3, v2, v0
	v_or_b32_e32 v196, v1, v0
	v_bitop3_b32 v2, v2, 64, v0 bitop3:0x36
	v_bitop3_b32 v197, v1, 64, v0 bitop3:0x36
	v_mov_b32_e32 v64, 0
	s_add_i32 s0, 0, 0x10000
	s_add_i32 s1, 0, 0x14000
	s_add_i32 s43, s25, 0xc000
	s_add_i32 s44, s25, 0xe000
	s_mov_b32 s45, -2
	s_mov_b64 s[14:15], 0
	v_add_u32_e32 v198, 0, v3
	v_add_u32_e32 v199, 0, v2
	s_add_i32 s46, 0, 0x18000
	v_mov_b32_e32 v65, v64
	v_mov_b32_e32 v66, v64
	v_mov_b32_e32 v67, v64
	v_mov_b32_e32 v68, v64
	v_mov_b32_e32 v69, v64
	v_mov_b32_e32 v70, v64
	v_mov_b32_e32 v71, v64
	v_mov_b32_e32 v76, v64
	v_mov_b32_e32 v77, v64
	v_mov_b32_e32 v78, v64
	v_mov_b32_e32 v79, v64
	v_mov_b32_e32 v80, v64
	v_mov_b32_e32 v81, v64
	v_mov_b32_e32 v82, v64
	v_mov_b32_e32 v83, v64
	v_mov_b32_e32 v88, v64
	v_mov_b32_e32 v89, v64
	v_mov_b32_e32 v90, v64
	v_mov_b32_e32 v91, v64
	v_mov_b32_e32 v92, v64
	v_mov_b32_e32 v93, v64
	v_mov_b32_e32 v94, v64
	v_mov_b32_e32 v95, v64
	v_mov_b32_e32 v104, v64
	v_mov_b32_e32 v105, v64
	v_mov_b32_e32 v106, v64
	v_mov_b32_e32 v107, v64
	v_mov_b32_e32 v108, v64
	v_mov_b32_e32 v109, v64
	v_mov_b32_e32 v110, v64
	v_mov_b32_e32 v111, v64
	v_mov_b32_e32 v72, v64
	v_mov_b32_e32 v73, v64
	v_mov_b32_e32 v74, v64
	v_mov_b32_e32 v75, v64
	v_mov_b32_e32 v84, v64
	v_mov_b32_e32 v85, v64
	v_mov_b32_e32 v86, v64
	v_mov_b32_e32 v87, v64
	v_mov_b32_e32 v96, v64
	v_mov_b32_e32 v97, v64
	v_mov_b32_e32 v98, v64
	v_mov_b32_e32 v99, v64
	v_mov_b32_e32 v100, v64
	v_mov_b32_e32 v101, v64
	v_mov_b32_e32 v102, v64
	v_mov_b32_e32 v103, v64
	v_mov_b32_e32 v112, v64
	v_mov_b32_e32 v113, v64
	v_mov_b32_e32 v114, v64
	v_mov_b32_e32 v115, v64
	v_mov_b32_e32 v116, v64
	v_mov_b32_e32 v117, v64
	v_mov_b32_e32 v118, v64
	v_mov_b32_e32 v119, v64
	v_mov_b32_e32 v120, v64
	v_mov_b32_e32 v121, v64
	v_mov_b32_e32 v122, v64
	v_mov_b32_e32 v123, v64
	v_mov_b32_e32 v124, v64
	v_mov_b32_e32 v125, v64
	v_mov_b32_e32 v126, v64
	v_mov_b32_e32 v127, v64
	v_mov_b32_e32 v128, v64
	v_mov_b32_e32 v129, v64
	v_mov_b32_e32 v130, v64
	v_mov_b32_e32 v131, v64
	v_mov_b32_e32 v132, v64
	v_mov_b32_e32 v133, v64
	v_mov_b32_e32 v134, v64
	v_mov_b32_e32 v135, v64
	v_mov_b32_e32 v140, v64
	v_mov_b32_e32 v141, v64
	v_mov_b32_e32 v142, v64
	v_mov_b32_e32 v143, v64
	v_mov_b32_e32 v148, v64
	v_mov_b32_e32 v149, v64
	v_mov_b32_e32 v150, v64
	v_mov_b32_e32 v151, v64
	v_mov_b32_e32 v156, v64
	v_mov_b32_e32 v157, v64
	v_mov_b32_e32 v158, v64
	v_mov_b32_e32 v159, v64
	v_mov_b32_e32 v164, v64
	v_mov_b32_e32 v165, v64
	v_mov_b32_e32 v166, v64
	v_mov_b32_e32 v167, v64
	v_mov_b32_e32 v172, v64
	v_mov_b32_e32 v173, v64
	v_mov_b32_e32 v174, v64
	v_mov_b32_e32 v175, v64
	v_mov_b32_e32 v180, v64
	v_mov_b32_e32 v181, v64
	v_mov_b32_e32 v182, v64
	v_mov_b32_e32 v183, v64
	v_mov_b32_e32 v136, v64
	v_mov_b32_e32 v137, v64
	v_mov_b32_e32 v138, v64
	v_mov_b32_e32 v139, v64
	v_mov_b32_e32 v144, v64
	v_mov_b32_e32 v145, v64
	v_mov_b32_e32 v146, v64
	v_mov_b32_e32 v147, v64
	v_mov_b32_e32 v152, v64
	v_mov_b32_e32 v153, v64
	v_mov_b32_e32 v154, v64
	v_mov_b32_e32 v155, v64
	v_mov_b32_e32 v160, v64
	v_mov_b32_e32 v161, v64
	v_mov_b32_e32 v162, v64
	v_mov_b32_e32 v163, v64
	v_mov_b32_e32 v168, v64
	v_mov_b32_e32 v169, v64
	v_mov_b32_e32 v170, v64
	v_mov_b32_e32 v171, v64
	v_mov_b32_e32 v176, v64
	v_mov_b32_e32 v177, v64
	v_mov_b32_e32 v178, v64
	v_mov_b32_e32 v179, v64
	v_mov_b32_e32 v184, v64
	v_mov_b32_e32 v185, v64
	v_mov_b32_e32 v186, v64
	v_mov_b32_e32 v187, v64
	v_mov_b32_e32 v188, v64
	v_mov_b32_e32 v189, v64
	v_mov_b32_e32 v190, v64
	v_mov_b32_e32 v191, v64
	v_add_u32_e32 v200, s0, v196
	v_add_u32_e32 v201, s0, v197
	v_add_u32_e32 v202, s1, v196
	v_add_u32_e32 v203, s1, v197
	s_barrier
	s_cmpk_eq_i32 s14, 0x700
	s_cselect_b64 s[18:19], -1, 0
	s_cmpk_lg_i32 s14, 0x700
	s_cselect_b64 s[26:27], -1, 0
	s_add_u32 s50, s16, s14
	s_addc_u32 s51, s13, s15
	s_add_u32 s47, s12, s14
	s_addc_u32 s48, s7, s15
	s_add_u32 s20, s47, 0x100
	s_addc_u32 s49, s48, 0
	s_add_u32 s8, s50, 0x40080
	s_addc_u32 s0, s51, 0
	s_and_b32 s9, s0, 0xffff
	v_add_u32_e32 v205, 0x1c000, v196
	v_add_u32_e32 v206, 0x1c000, v197
	s_branch .LBB5_18
	.p2align	6
